# router top-4 selection spread over 4 lanes per token (quad DPP merge) instead of one wave's serial LDS scan
# speedup vs baseline: 1.0063x; 1.0063x over previous
; #define LAS __attribute__((address_space(3)))
; #define lds lds_hidden(lds0)
; __device__ __forceinline__ void router_phase(LAS unsigned char* lds, const bf16_t* __restrict__ X, const float* __restrict__ gain, const float* __restrict__ mod_l, ...
;     ...
;         f32x16 acc0, acc1;
; #pragma unroll
;         for (int i = 0; i < 16; ++i) { acc0[i] = 0.f; acc1[i] = 0.f; }
; #pragma unroll
;         for (int i = 0; i < 8; ++i) {
;             const bf16x8 a0 = *(const LAS bf16x8*)(lds + r31 * XRB + (wid * 128 + i * 16 + kg * 8) * 2);
;             const bf16x8 a1 = *(const LAS bf16x8*)(lds + (32 + r31) * XRB + (wid * 128 + i * 16 + kg * 8) * 2);
;             acc0 = __builtin_amdgcn_mfma_f32_32x32x16_bf16(a0, bh[i], acc0, 0, 0, 0);
;             acc1 = __builtin_amdgcn_mfma_f32_32x32x16_bf16(a1, bh[i], acc1, 0, 0, 0);
;             acc0 = __builtin_amdgcn_mfma_f32_32x32x16_bf16(a0, bl[i], acc0, 0, 0, 0);
;             acc1 = __builtin_amdgcn_mfma_f32_32x32x16_bf16(a1, bl[i], acc1, 0, 0, 0);
;         }
;         __syncthreads();
;         LAS float* part = (LAS float*)lds;
; #pragma unroll
;         for (int i = 0; i < 16; ++i) { part[(wid * 2 + 0) * 1024 + i * 64 + lane] = acc0[i]; part[(wid * 2 + 1) * 1024 + i * 64 + lane] = acc1[i]; }
;         __syncthreads();
; #pragma unroll
;         for (int j = 0; j < 4; ++j) {
;             const int o = tid + j * 512, rg = o >> 10, reg = (o >> 6) & 15, ln = o & 63;
;             float sm = 0.f;
; #pragma unroll
;             for (int w = 0; w < 8; ++w) sm += part[(w * 2 + rg) * 1024 + reg * 64 + ln];
;             const int e = ln & 31, row = rg * 32 + (reg & 3) + 8 * (reg >> 2) + 4 * (ln >> 5);
;             lg[row * 33 + e] = sm * rs[row] + BRP_l[b * NE + e];
;         }
;         __syncthreads();
.LBB0_1273:
	v_add_u32_e32 v130, v162, v163
	v_add_u32_e32 v22, v164, v163
	ds_read_b128 v[112:115], v130
	ds_read_b128 v[126:129], v22
	s_waitcnt vmcnt(17) lgkmcnt(1)
	v_mfma_f32_32x32x16_bf16 v[2:17], v[112:115], v[18:21], 0
	s_waitcnt lgkmcnt(0)
	v_mfma_f32_32x32x16_bf16 v[18:33], v[126:129], v[18:21], 0
	s_waitcnt vmcnt(16)
	v_mfma_f32_32x32x16_bf16 v[2:17], v[112:115], v[108:111], v[2:17]
	ds_read_b128 v[112:115], v225
	v_mfma_f32_32x32x16_bf16 v[18:33], v[126:129], v[108:111], v[18:33]
	ds_read_b128 v[108:111], v130 offset:32
	s_waitcnt vmcnt(14) lgkmcnt(0)
	v_mfma_f32_32x32x16_bf16 v[2:17], v[108:111], v[104:107], v[2:17]
	v_mfma_f32_32x32x16_bf16 v[18:33], v[112:115], v[104:107], v[18:33]
	ds_read_b128 v[104:107], v226
	v_mfma_f32_32x32x16_bf16 v[2:17], v[108:111], v[92:95], v[2:17]
	v_mfma_f32_32x32x16_bf16 v[18:33], v[112:115], v[92:95], v[18:33]
	ds_read_b128 v[92:95], v130 offset:64
	s_waitcnt vmcnt(12) lgkmcnt(0)
	v_mfma_f32_32x32x16_bf16 v[2:17], v[92:95], v[96:99], v[2:17]
	v_mfma_f32_32x32x16_bf16 v[18:33], v[104:107], v[96:99], v[18:33]
	ds_read_b128 v[96:99], v227
	v_mfma_f32_32x32x16_bf16 v[2:17], v[92:95], v[100:103], v[2:17]
	ds_read_b128 v[92:95], v130 offset:96
	v_mfma_f32_32x32x16_bf16 v[18:33], v[104:107], v[100:103], v[18:33]
	s_waitcnt vmcnt(10) lgkmcnt(0)
	v_mfma_f32_32x32x16_bf16 v[2:17], v[92:95], v[88:91], v[2:17]
	v_mfma_f32_32x32x16_bf16 v[18:33], v[96:99], v[88:91], v[18:33]
	ds_read_b128 v[88:91], v228
	v_mfma_f32_32x32x16_bf16 v[2:17], v[92:95], v[76:79], v[2:17]
	v_mfma_f32_32x32x16_bf16 v[18:33], v[96:99], v[76:79], v[18:33]
	ds_read_b128 v[76:79], v130 offset:128
	s_waitcnt vmcnt(8) lgkmcnt(0)
	v_mfma_f32_32x32x16_bf16 v[2:17], v[76:79], v[80:83], v[2:17]
	v_mfma_f32_32x32x16_bf16 v[18:33], v[88:91], v[80:83], v[18:33]
	ds_read_b128 v[80:83], v229
	v_mfma_f32_32x32x16_bf16 v[2:17], v[76:79], v[84:87], v[2:17]
	ds_read_b128 v[76:79], v130 offset:160
	v_mfma_f32_32x32x16_bf16 v[18:33], v[88:91], v[84:87], v[18:33]
	s_waitcnt vmcnt(6) lgkmcnt(0)
	v_mfma_f32_32x32x16_bf16 v[2:17], v[76:79], v[72:75], v[2:17]
	v_mfma_f32_32x32x16_bf16 v[18:33], v[80:83], v[72:75], v[18:33]
	ds_read_b128 v[72:75], v230
	v_mfma_f32_32x32x16_bf16 v[2:17], v[76:79], v[60:63], v[2:17]
	v_mfma_f32_32x32x16_bf16 v[18:33], v[80:83], v[60:63], v[18:33]
	ds_read_b128 v[60:63], v130 offset:192
	s_waitcnt vmcnt(4) lgkmcnt(0)
	v_mfma_f32_32x32x16_bf16 v[2:17], v[60:63], v[64:67], v[2:17]
	v_mfma_f32_32x32x16_bf16 v[18:33], v[72:75], v[64:67], v[18:33]
	ds_read_b128 v[64:67], v231
	v_mfma_f32_32x32x16_bf16 v[2:17], v[60:63], v[68:71], v[2:17]
	ds_read_b128 v[60:63], v130 offset:224
	s_waitcnt lgkmcnt(0)
	s_barrier
	v_mfma_f32_32x32x16_bf16 v[18:33], v[72:75], v[68:71], v[18:33]
	s_waitcnt vmcnt(3)
	v_mfma_f32_32x32x16_bf16 v[2:17], v[60:63], v[56:59], v[2:17]
	v_mfma_f32_32x32x16_bf16 v[18:33], v[64:67], v[56:59], v[18:33]
	s_waitcnt vmcnt(2)
	v_mfma_f32_32x32x16_bf16 v[2:17], v[60:63], v[52:55], v[2:17]
	v_mfma_f32_32x32x16_bf16 v[18:33], v[64:67], v[52:55], v[18:33]
	s_nop 10
	ds_write2st64_b32 v232, v2, v3 offset1:1
	v_lshl_or_b32 v2, s0, 5, v119
	v_ashrrev_i32_e32 v3, 31, v2
	v_lshl_add_u64 v[2:3], v[2:3], 2, s[26:27]
	ds_write2st64_b32 v232, v18, v19 offset0:16 offset1:17
	ds_write2st64_b32 v232, v4, v5 offset0:2 offset1:3
	ds_write2st64_b32 v232, v20, v21 offset0:18 offset1:19
	ds_write2st64_b32 v232, v6, v7 offset0:4 offset1:5
	ds_write2st64_b32 v232, v22, v23 offset0:20 offset1:21
	ds_write2st64_b32 v232, v8, v9 offset0:6 offset1:7
	ds_write2st64_b32 v232, v24, v25 offset0:22 offset1:23
	ds_write2st64_b32 v232, v10, v11 offset0:8 offset1:9
	ds_write2st64_b32 v232, v26, v27 offset0:24 offset1:25
	ds_write2st64_b32 v232, v12, v13 offset0:10 offset1:11
	ds_write2st64_b32 v232, v28, v29 offset0:26 offset1:27
	ds_write2st64_b32 v232, v14, v15 offset0:12 offset1:13
	ds_write2st64_b32 v232, v30, v31 offset0:28 offset1:29
	ds_write2st64_b32 v232, v16, v17 offset0:14 offset1:15
	ds_write2st64_b32 v232, v32, v33 offset0:30 offset1:31
	s_waitcnt lgkmcnt(0)
	s_barrier
	global_load_dword v10, v[2:3], off
	ds_read2st64_b32 v[2:3], v188 offset1:32
	ds_read2st64_b32 v[4:5], v188 offset0:64 offset1:96
	s_waitcnt lgkmcnt(1)
	v_add_f32_e32 v2, 0, v2
	v_add_f32_e32 v6, v2, v3
	ds_read2st64_b32 v[2:3], v188 offset0:128 offset1:160
	s_waitcnt lgkmcnt(1)
	v_add_f32_e32 v4, v6, v4
	ds_read2st64_b32 v[6:7], v188 offset0:192 offset1:224
	v_add_f32_e32 v4, v4, v5
	ds_read_b32 v5, v189
	s_waitcnt lgkmcnt(2)
	v_add_f32_e32 v2, v4, v2
	v_add_f32_e32 v2, v2, v3
	s_waitcnt lgkmcnt(1)
	v_add_f32_e32 v2, v2, v6
	v_add_f32_e32 v2, v2, v7
	s_waitcnt vmcnt(0) lgkmcnt(0)
	v_fma_f32 v2, v2, v5, v10
	ds_write_b32 v233, v2
	ds_read2st64_b32 v[2:3], v190 offset1:32
	ds_read2st64_b32 v[4:5], v190 offset0:64 offset1:96
	s_waitcnt lgkmcnt(1)
	v_add_f32_e32 v2, 0, v2
	v_add_f32_e32 v6, v2, v3
	ds_read2st64_b32 v[2:3], v190 offset0:128 offset1:160
	s_waitcnt lgkmcnt(1)
	v_add_f32_e32 v4, v6, v4
	ds_read2st64_b32 v[6:7], v190 offset0:192 offset1:224
	v_add_f32_e32 v4, v4, v5
	ds_read_b32 v5, v191
	s_waitcnt lgkmcnt(2)
	v_add_f32_e32 v2, v4, v2
	v_add_f32_e32 v2, v2, v3
	s_waitcnt lgkmcnt(1)
	v_add_f32_e32 v2, v2, v6
	v_add_f32_e32 v2, v2, v7
	s_waitcnt lgkmcnt(0)
	v_fma_f32 v2, v2, v5, v10
	ds_write_b32 v234, v2
	ds_read2st64_b32 v[2:3], v192 offset1:32
	ds_read2st64_b32 v[4:5], v192 offset0:64 offset1:96
	s_waitcnt lgkmcnt(1)
	v_add_f32_e32 v2, 0, v2
	v_add_f32_e32 v6, v2, v3
	ds_read2st64_b32 v[2:3], v192 offset0:128 offset1:160
	s_waitcnt lgkmcnt(1)
	v_add_f32_e32 v4, v6, v4
	ds_read2st64_b32 v[6:7], v192 offset0:192 offset1:224
	v_add_f32_e32 v4, v4, v5
	ds_read_b32 v5, v193
	s_waitcnt lgkmcnt(2)
	v_add_f32_e32 v2, v4, v2
	v_add_f32_e32 v2, v2, v3
	s_waitcnt lgkmcnt(1)
	v_add_f32_e32 v2, v2, v6
	v_add_f32_e32 v2, v2, v7
	s_waitcnt lgkmcnt(0)
	v_fma_f32 v2, v2, v5, v10
	ds_write_b32 v235, v2
	ds_read2st64_b32 v[2:3], v194 offset1:32
	ds_read2st64_b32 v[4:5], v194 offset0:64 offset1:96
	ds_read2st64_b32 v[6:7], v194 offset0:128 offset1:160
	ds_read2st64_b32 v[8:9], v194 offset0:192 offset1:224
	ds_read_b32 v11, v195
	s_waitcnt lgkmcnt(4)
	v_add_f32_e32 v2, 0, v2
	v_add_f32_e32 v2, v2, v3
	s_waitcnt lgkmcnt(3)
	v_add_f32_e32 v2, v2, v4
	v_add_f32_e32 v2, v2, v5
	s_waitcnt lgkmcnt(2)
	v_add_f32_e32 v2, v2, v6
	v_add_f32_e32 v2, v2, v7
	s_waitcnt lgkmcnt(1)
	v_add_f32_e32 v2, v2, v8
	v_add_f32_e32 v2, v2, v9
	s_waitcnt lgkmcnt(0)
	v_fmac_f32_e32 v10, v2, v11
	ds_write_b32 v236, v10
	s_waitcnt lgkmcnt(0)
	s_barrier
; __device__ __forceinline__ float fexp(float x) { return __builtin_amdgcn_exp2f(x * 1.4426950408889634f); }
; __device__ __forceinline__ float kf(float x) { asm volatile("" : "+s"(x)); return x; }
; __device__ __forceinline__ void router_phase(LAS unsigned char* lds, const bf16_t* __restrict__ X, const float* __restrict__ gain, const float* __restrict__ mod_l, ...
;     ...
;         if (tid < 64) {
;             const int row = tid; unsigned used = 0u; int idx[4]; float val[4];
; #pragma unroll
;             for (int k = 0; k < 4; ++k) {
;                 float bv = kf(-3.0e38f); int bi = 0;
;                 for (int e = 0; e < 32; ++e) { const float v = lg[row * 33 + e]; if (!((used >> e) & 1u) && v > bv) { bv = v; bi = e; } }
;                 used |= 1u << bi; idx[k] = bi; val[k] = bv;
;             }
;             float ex[4], sm = 0.f;
; #pragma unroll
;             for (int k = 0; k < 4; ++k) { ex[k] = fexp(val[k] - val[0]); sm += ex[k]; }
; #pragma unroll
;             for (int k = 0; k < 4; ++k) {
;                 const int slot = row * 4 + k;
;                 se[slot] = idx[k]; sg[slot] = ex[k] / sm; sr[slot] = __hip_atomic_fetch_add(&lc[idx[k]], 1, __ATOMIC_RELAXED, __HIP_MEMORY_SCOPE_WORKGROUP);
;             }
	s_and_saveexec_b64 s[28:29], s[10:11]
	s_cbranch_execz .LBB0_1275
	v_lshrrev_b32_e32 v2, 2, v0
	v_and_b32_e32 v3, 3, v0
	s_movk_i32 s0, 0x84
	v_mul_u32_u24_e32 v4, s0, v2
	v_lshl_add_u32 v4, v3, 5, v4
	s_add_i32 s0, s36, 0xffffd300
	v_add_u32_e32 v4, s0, v4
	ds_read2_b32 v[52:53], v4 offset0:0 offset1:1
	ds_read2_b32 v[54:55], v4 offset0:2 offset1:3
	ds_read2_b32 v[56:57], v4 offset0:4 offset1:5
	ds_read2_b32 v[58:59], v4 offset0:6 offset1:7
	v_lshlrev_b32_e32 v60, 3, v3
	v_or_b32_e32 v61, 1, v60
	v_or_b32_e32 v62, 2, v60
	v_or_b32_e32 v63, 3, v60
	v_or_b32_e32 v64, 4, v60
	v_or_b32_e32 v65, 5, v60
	v_or_b32_e32 v66, 6, v60
	v_or_b32_e32 v67, 7, v60
	v_mov_b32_e32 v6, 0xff61b1e6
	s_waitcnt lgkmcnt(0)
	v_cmp_gt_f32_e32 vcc, v53, v52
	v_cmp_gt_f32_e64 s[12:13], v55, v54
	v_cmp_gt_f32_e64 s[0:1], v57, v56
	v_cndmask_b32_e32 v8, v52, v53, vcc
	v_cndmask_b32_e32 v9, v60, v61, vcc
	v_cmp_gt_f32_e32 vcc, v59, v58
	v_cndmask_b32_e64 v10, v54, v55, s[12:13]
	v_cndmask_b32_e64 v11, v62, v63, s[12:13]
	v_cndmask_b32_e64 v68, v56, v57, s[0:1]
	v_cndmask_b32_e64 v69, v64, v65, s[0:1]
	v_cndmask_b32_e32 v70, v58, v59, vcc
	v_cndmask_b32_e32 v71, v66, v67, vcc
	v_cmp_gt_f32_e32 vcc, v10, v8
	v_cmp_gt_f32_e64 s[12:13], v70, v68
	s_nop 0
	v_cndmask_b32_e32 v8, v8, v10, vcc
	v_cndmask_b32_e32 v9, v9, v11, vcc
	v_cndmask_b32_e64 v68, v68, v70, s[12:13]
	v_cndmask_b32_e64 v69, v69, v71, s[12:13]
	v_cmp_gt_f32_e32 vcc, v68, v8
	s_nop 1
	v_cndmask_b32_e32 v8, v8, v68, vcc
	v_cndmask_b32_e32 v9, v9, v69, vcc
	s_nop 0
	v_mov_b32_dpp v10, v8 quad_perm:[1,0,3,2] row_mask:0xf bank_mask:0xf
	v_mov_b32_dpp v11, v9 quad_perm:[1,0,3,2] row_mask:0xf bank_mask:0xf
	v_cmp_gt_f32_e32 vcc, v10, v8
	v_cmp_eq_f32_e64 s[12:13], v10, v8
	v_cmp_lt_u32_e64 s[0:1], v11, v9
	s_and_b64 s[12:13], s[12:13], s[0:1]
	s_or_b64 vcc, vcc, s[12:13]
	v_cndmask_b32_e32 v8, v8, v10, vcc
	v_cndmask_b32_e32 v9, v9, v11, vcc
	s_nop 0
	v_mov_b32_dpp v10, v8 quad_perm:[2,3,0,1] row_mask:0xf bank_mask:0xf
	v_mov_b32_dpp v11, v9 quad_perm:[2,3,0,1] row_mask:0xf bank_mask:0xf
	v_cmp_gt_f32_e32 vcc, v10, v8
	v_cmp_eq_f32_e64 s[12:13], v10, v8
	v_cmp_lt_u32_e64 s[0:1], v11, v9
	s_and_b64 s[12:13], s[12:13], s[0:1]
	s_or_b64 vcc, vcc, s[12:13]
	v_cndmask_b32_e32 v72, v8, v10, vcc
	v_cndmask_b32_e32 v76, v9, v11, vcc
	v_cmp_eq_u32_e32 vcc, v76, v60
	v_cmp_eq_u32_e64 s[12:13], v76, v61
	v_cmp_eq_u32_e64 s[0:1], v76, v62
	v_cndmask_b32_e32 v52, v52, v6, vcc
	v_cmp_eq_u32_e32 vcc, v76, v63
	v_cndmask_b32_e64 v53, v53, v6, s[12:13]
	v_cndmask_b32_e64 v54, v54, v6, s[0:1]
	v_cndmask_b32_e32 v55, v55, v6, vcc
	v_cmp_eq_u32_e32 vcc, v76, v64
	v_cmp_eq_u32_e64 s[12:13], v76, v65
	v_cmp_eq_u32_e64 s[0:1], v76, v66
	v_cndmask_b32_e32 v56, v56, v6, vcc
	v_cmp_eq_u32_e32 vcc, v76, v67
	v_cndmask_b32_e64 v57, v57, v6, s[12:13]
	v_cndmask_b32_e64 v58, v58, v6, s[0:1]
	v_cndmask_b32_e32 v59, v59, v6, vcc
	v_cmp_gt_f32_e32 vcc, v53, v52
	v_cmp_gt_f32_e64 s[12:13], v55, v54
	v_cmp_gt_f32_e64 s[0:1], v57, v56
	v_cndmask_b32_e32 v8, v52, v53, vcc
	v_cndmask_b32_e32 v9, v60, v61, vcc
	v_cmp_gt_f32_e32 vcc, v59, v58
	v_cndmask_b32_e64 v10, v54, v55, s[12:13]
	v_cndmask_b32_e64 v11, v62, v63, s[12:13]
	v_cndmask_b32_e64 v68, v56, v57, s[0:1]
	v_cndmask_b32_e64 v69, v64, v65, s[0:1]
	v_cndmask_b32_e32 v70, v58, v59, vcc
	v_cndmask_b32_e32 v71, v66, v67, vcc
	v_cmp_gt_f32_e32 vcc, v10, v8
	v_cmp_gt_f32_e64 s[12:13], v70, v68
	s_nop 0
	v_cndmask_b32_e32 v8, v8, v10, vcc
	v_cndmask_b32_e32 v9, v9, v11, vcc
	v_cndmask_b32_e64 v68, v68, v70, s[12:13]
	v_cndmask_b32_e64 v69, v69, v71, s[12:13]
	v_cmp_gt_f32_e32 vcc, v68, v8
	s_nop 1
	v_cndmask_b32_e32 v8, v8, v68, vcc
	v_cndmask_b32_e32 v9, v9, v69, vcc
	s_nop 0
	v_mov_b32_dpp v10, v8 quad_perm:[1,0,3,2] row_mask:0xf bank_mask:0xf
	v_mov_b32_dpp v11, v9 quad_perm:[1,0,3,2] row_mask:0xf bank_mask:0xf
	v_cmp_gt_f32_e32 vcc, v10, v8
	v_cmp_eq_f32_e64 s[12:13], v10, v8
	v_cmp_lt_u32_e64 s[0:1], v11, v9
	s_and_b64 s[12:13], s[12:13], s[0:1]
	s_or_b64 vcc, vcc, s[12:13]
	v_cndmask_b32_e32 v8, v8, v10, vcc
	v_cndmask_b32_e32 v9, v9, v11, vcc
	s_nop 0
	v_mov_b32_dpp v10, v8 quad_perm:[2,3,0,1] row_mask:0xf bank_mask:0xf
	v_mov_b32_dpp v11, v9 quad_perm:[2,3,0,1] row_mask:0xf bank_mask:0xf
	v_cmp_gt_f32_e32 vcc, v10, v8
	v_cmp_eq_f32_e64 s[12:13], v10, v8
	v_cmp_lt_u32_e64 s[0:1], v11, v9
	s_and_b64 s[12:13], s[12:13], s[0:1]
	s_or_b64 vcc, vcc, s[12:13]
	v_cndmask_b32_e32 v73, v8, v10, vcc
	v_cndmask_b32_e32 v77, v9, v11, vcc
	v_cmp_eq_u32_e32 vcc, v77, v60
	v_cmp_eq_u32_e64 s[12:13], v77, v61
	v_cmp_eq_u32_e64 s[0:1], v77, v62
	v_cndmask_b32_e32 v52, v52, v6, vcc
	v_cmp_eq_u32_e32 vcc, v77, v63
	v_cndmask_b32_e64 v53, v53, v6, s[12:13]
	v_cndmask_b32_e64 v54, v54, v6, s[0:1]
	v_cndmask_b32_e32 v55, v55, v6, vcc
	v_cmp_eq_u32_e32 vcc, v77, v64
	v_cmp_eq_u32_e64 s[12:13], v77, v65
	v_cmp_eq_u32_e64 s[0:1], v77, v66
	v_cndmask_b32_e32 v56, v56, v6, vcc
	v_cmp_eq_u32_e32 vcc, v77, v67
	v_cndmask_b32_e64 v57, v57, v6, s[12:13]
	v_cndmask_b32_e64 v58, v58, v6, s[0:1]
	v_cndmask_b32_e32 v59, v59, v6, vcc
	v_cmp_gt_f32_e32 vcc, v53, v52
	v_cmp_gt_f32_e64 s[12:13], v55, v54
; __device__ __forceinline__ float fexp(float x) { return __builtin_amdgcn_exp2f(x * 1.4426950408889634f); }
; __device__ __forceinline__ float kf(float x) { asm volatile("" : "+s"(x)); return x; }
; __device__ __forceinline__ void router_phase(LAS unsigned char* lds, const bf16_t* __restrict__ X, const float* __restrict__ gain, const float* __restrict__ mod_l, ...
;     ...
;             const int row = tid; unsigned used = 0u; int idx[4]; float val[4];
; #pragma unroll
;             for (int k = 0; k < 4; ++k) {
;                 float bv = kf(-3.0e38f); int bi = 0;
;                 for (int e = 0; e < 32; ++e) { const float v = lg[row * 33 + e]; if (!((used >> e) & 1u) && v > bv) { bv = v; bi = e; } }
;                 used |= 1u << bi; idx[k] = bi; val[k] = bv;
;             }
;             float ex[4], sm = 0.f;
; #pragma unroll
;             for (int k = 0; k < 4; ++k) { ex[k] = fexp(val[k] - val[0]); sm += ex[k]; }
; #pragma unroll
;             for (int k = 0; k < 4; ++k) {
;                 const int slot = row * 4 + k;
;                 se[slot] = idx[k]; sg[slot] = ex[k] / sm; sr[slot] = __hip_atomic_fetch_add(&lc[idx[k]], 1, __ATOMIC_RELAXED, __HIP_MEMORY_SCOPE_WORKGROUP);
;             }
	v_cmp_gt_f32_e64 s[0:1], v57, v56
	v_cndmask_b32_e32 v8, v52, v53, vcc
	v_cndmask_b32_e32 v9, v60, v61, vcc
	v_cmp_gt_f32_e32 vcc, v59, v58
	v_cndmask_b32_e64 v10, v54, v55, s[12:13]
	v_cndmask_b32_e64 v11, v62, v63, s[12:13]
	v_cndmask_b32_e64 v68, v56, v57, s[0:1]
	v_cndmask_b32_e64 v69, v64, v65, s[0:1]
	v_cndmask_b32_e32 v70, v58, v59, vcc
	v_cndmask_b32_e32 v71, v66, v67, vcc
	v_cmp_gt_f32_e32 vcc, v10, v8
	v_cmp_gt_f32_e64 s[12:13], v70, v68
	s_nop 0
	v_cndmask_b32_e32 v8, v8, v10, vcc
	v_cndmask_b32_e32 v9, v9, v11, vcc
	v_cndmask_b32_e64 v68, v68, v70, s[12:13]
	v_cndmask_b32_e64 v69, v69, v71, s[12:13]
	v_cmp_gt_f32_e32 vcc, v68, v8
	s_nop 1
	v_cndmask_b32_e32 v8, v8, v68, vcc
	v_cndmask_b32_e32 v9, v9, v69, vcc
	s_nop 0
	v_mov_b32_dpp v10, v8 quad_perm:[1,0,3,2] row_mask:0xf bank_mask:0xf
	v_mov_b32_dpp v11, v9 quad_perm:[1,0,3,2] row_mask:0xf bank_mask:0xf
	v_cmp_gt_f32_e32 vcc, v10, v8
	v_cmp_eq_f32_e64 s[12:13], v10, v8
	v_cmp_lt_u32_e64 s[0:1], v11, v9
	s_and_b64 s[12:13], s[12:13], s[0:1]
	s_or_b64 vcc, vcc, s[12:13]
	v_cndmask_b32_e32 v8, v8, v10, vcc
	v_cndmask_b32_e32 v9, v9, v11, vcc
	s_nop 0
	v_mov_b32_dpp v10, v8 quad_perm:[2,3,0,1] row_mask:0xf bank_mask:0xf
	v_mov_b32_dpp v11, v9 quad_perm:[2,3,0,1] row_mask:0xf bank_mask:0xf
	v_cmp_gt_f32_e32 vcc, v10, v8
	v_cmp_eq_f32_e64 s[12:13], v10, v8
	v_cmp_lt_u32_e64 s[0:1], v11, v9
	s_and_b64 s[12:13], s[12:13], s[0:1]
	s_or_b64 vcc, vcc, s[12:13]
	v_cndmask_b32_e32 v74, v8, v10, vcc
	v_cndmask_b32_e32 v78, v9, v11, vcc
	v_cmp_eq_u32_e32 vcc, v78, v60
	v_cmp_eq_u32_e64 s[12:13], v78, v61
	v_cmp_eq_u32_e64 s[0:1], v78, v62
	v_cndmask_b32_e32 v52, v52, v6, vcc
	v_cmp_eq_u32_e32 vcc, v78, v63
	v_cndmask_b32_e64 v53, v53, v6, s[12:13]
	v_cndmask_b32_e64 v54, v54, v6, s[0:1]
	v_cndmask_b32_e32 v55, v55, v6, vcc
	v_cmp_eq_u32_e32 vcc, v78, v64
	v_cmp_eq_u32_e64 s[12:13], v78, v65
	v_cmp_eq_u32_e64 s[0:1], v78, v66
	v_cndmask_b32_e32 v56, v56, v6, vcc
	v_cmp_eq_u32_e32 vcc, v78, v67
	v_cndmask_b32_e64 v57, v57, v6, s[12:13]
	v_cndmask_b32_e64 v58, v58, v6, s[0:1]
	v_cndmask_b32_e32 v59, v59, v6, vcc
	v_cmp_gt_f32_e32 vcc, v53, v52
	v_cmp_gt_f32_e64 s[12:13], v55, v54
	v_cmp_gt_f32_e64 s[0:1], v57, v56
	v_cndmask_b32_e32 v8, v52, v53, vcc
	v_cndmask_b32_e32 v9, v60, v61, vcc
	v_cmp_gt_f32_e32 vcc, v59, v58
	v_cndmask_b32_e64 v10, v54, v55, s[12:13]
	v_cndmask_b32_e64 v11, v62, v63, s[12:13]
	v_cndmask_b32_e64 v68, v56, v57, s[0:1]
	v_cndmask_b32_e64 v69, v64, v65, s[0:1]
	v_cndmask_b32_e32 v70, v58, v59, vcc
	v_cndmask_b32_e32 v71, v66, v67, vcc
	v_cmp_gt_f32_e32 vcc, v10, v8
	v_cmp_gt_f32_e64 s[12:13], v70, v68
	s_nop 0
	v_cndmask_b32_e32 v8, v8, v10, vcc
	v_cndmask_b32_e32 v9, v9, v11, vcc
	v_cndmask_b32_e64 v68, v68, v70, s[12:13]
	v_cndmask_b32_e64 v69, v69, v71, s[12:13]
	v_cmp_gt_f32_e32 vcc, v68, v8
	s_nop 1
	v_cndmask_b32_e32 v8, v8, v68, vcc
	v_cndmask_b32_e32 v9, v9, v69, vcc
	s_nop 0
	v_mov_b32_dpp v10, v8 quad_perm:[1,0,3,2] row_mask:0xf bank_mask:0xf
	v_mov_b32_dpp v11, v9 quad_perm:[1,0,3,2] row_mask:0xf bank_mask:0xf
	v_cmp_gt_f32_e32 vcc, v10, v8
	v_cmp_eq_f32_e64 s[12:13], v10, v8
	v_cmp_lt_u32_e64 s[0:1], v11, v9
	s_and_b64 s[12:13], s[12:13], s[0:1]
	s_or_b64 vcc, vcc, s[12:13]
	v_cndmask_b32_e32 v8, v8, v10, vcc
	v_cndmask_b32_e32 v9, v9, v11, vcc
	s_nop 0
	v_mov_b32_dpp v10, v8 quad_perm:[2,3,0,1] row_mask:0xf bank_mask:0xf
	v_mov_b32_dpp v11, v9 quad_perm:[2,3,0,1] row_mask:0xf bank_mask:0xf
	v_cmp_gt_f32_e32 vcc, v10, v8
	v_cmp_eq_f32_e64 s[12:13], v10, v8
	v_cmp_lt_u32_e64 s[0:1], v11, v9
	s_and_b64 s[12:13], s[12:13], s[0:1]
	s_or_b64 vcc, vcc, s[12:13]
	v_cndmask_b32_e32 v75, v8, v10, vcc
	v_cndmask_b32_e32 v79, v9, v11, vcc
	v_sub_f32_e32 v80, v72, v72
	v_sub_f32_e32 v81, v73, v72
	v_sub_f32_e32 v82, v74, v72
	v_sub_f32_e32 v83, v75, v72
	v_mul_f32_e32 v80, 0x3fb8aa3b, v80
	v_mul_f32_e32 v81, 0x3fb8aa3b, v81
	v_mul_f32_e32 v82, 0x3fb8aa3b, v82
	v_mul_f32_e32 v83, 0x3fb8aa3b, v83
	v_exp_f32_e32 v80, v80
	v_exp_f32_e32 v81, v81
	v_exp_f32_e32 v82, v82
	v_exp_f32_e32 v83, v83
	v_cmp_eq_u32_e32 vcc, 1, v3
	v_cmp_eq_u32_e64 s[12:13], 2, v3
	v_cmp_eq_u32_e64 s[0:1], 3, v3
	v_add_f32_e32 v84, 0, v80
	v_add_f32_e32 v84, v84, v81
	v_add_f32_e32 v84, v84, v82
	v_add_f32_e32 v84, v84, v83
	v_cndmask_b32_e32 v85, v80, v81, vcc
	v_cndmask_b32_e32 v86, v76, v77, vcc
	v_cndmask_b32_e64 v85, v85, v82, s[12:13]
	v_cndmask_b32_e64 v86, v86, v78, s[12:13]
	v_cndmask_b32_e64 v85, v85, v83, s[0:1]
	v_cndmask_b32_e64 v86, v86, v79, s[0:1]
	v_div_scale_f32 v87, s[0:1], v84, v84, v85
	v_rcp_f32_e32 v88, v87
	s_nop 0
	v_fma_f32 v89, -v87, v88, 1.0
	v_fmac_f32_e32 v88, v89, v88
	v_div_scale_f32 v89, vcc, v85, v84, v85
	v_mul_f32_e32 v90, v89, v88
	v_fma_f32 v91, -v87, v90, v89
	v_fmac_f32_e32 v90, v91, v88
	v_fma_f32 v87, -v87, v90, v89
	v_div_fmas_f32 v87, v87, v88, v90
	v_div_fixup_f32 v92, v87, v84, v85
	s_add_i32 s0, s36, 0xfffff400
	v_lshl_add_u32 v4, v0, 2, s0
	v_lshl_add_u32 v5, v86, 2, s36
	ds_write_b32 v4, v86
	ds_write_b32 v4, v92 offset:1024
	ds_add_rtn_u32 v5, v5, v1
	s_waitcnt lgkmcnt(0)
	ds_write_b32 v4, v5 offset:2048
